# P1 epilogue: z tile stores with nt policy (streaming output no longer displaces the GEMM operand tiles in L2)
# speedup vs baseline: 1.0134x; 1.0092x over previous
; __device__ __forceinline__ unsigned cvt_pk_bf16(float lo, float hi) { unsigned r; asm volatile("v_cvt_pk_bf16_f32 %0, %1, %2" : "=v"(r) : "v"(lo), "v"(hi)); return r; }
; __device__ __forceinline__ float fast_sigmoid(float x) { return __builtin_amdgcn_rcpf(1.0f + __builtin_amdgcn_exp2f(-1.44269504089f * x)); }
;     __device__ __forceinline__ void operator()(const f32x4 (&acc)[2][2][4][2], const Unit& u, int wr, int wc, int fr_, int fq_) const {
;     ...
;         const int row0 = u.pm * BM + wr * 64 + fr, col0 = colt + wc * 32 + 8 * fq;
; #pragma unroll
;         for (int ai = 0; ai < 2; ++ai)
; #pragma unroll
;             for (int m = 0; m < 4; ++m) { bf16_t* rowp = base + (size_t)(row0 + ai * HALF + m * 16) * ldc + col0;
; #pragma unroll
;                 for (int bj = 0; bj < 2; ++bj) { f32x4 v0 = acc[ai][bj][m][0], v1 = acc[ai][bj][m][1];
;                     if (sig) {
; #pragma unroll
;                         for (int j = 0; j < 4; ++j) { v0[j] = fast_sigmoid(v0[j]); v1[j] = fast_sigmoid(v1[j]); } }
;                     u32x4 w; w.x = cvt_pk_bf16(v0[0], v0[1]); w.y = cvt_pk_bf16(v0[2], v0[3]); w.z = cvt_pk_bf16(v1[0], v1[1]); w.w = cvt_pk_bf16(v1[2], v1[3]);
;                     *(u32x4*)(rowp + bj * HALF) = w; } }
;     ...
;         if constexpr (F8 == 2) { const float dq_ = g.dq;
;             _Pragma("unroll") for (int a_ = 0; a_ < 2; ++a_) _Pragma("unroll") for (int b_ = 0; b_ < 2; ++b_) _Pragma("unroll") for (int m_ = 0; m_ < 4; ++m_) _Pragma("unroll") for (int n_ = 0; n_ < 2; ++n_) { const i32x4 c_ = __builtin_bit_cast(i32x4, acc[a_][b_][m_][n_]);
;                 acc[a_][b_][m_][n_] = (f32x4){(float)c_.x * dq_, (float)c_.y * dq_, (float)c_.z * dq_, (float)c_.w * dq_}; } }
.LBB0_126:
	v_ashrrev_i32_e32 v122, 1, v146
	v_and_b32_e32 v122, -8, v122
	s_add_i32 s61, s61, s93
	v_and_or_b32 v123, v146, 15, s92
	v_add_u32_e32 v122, s61, v122
	v_lshl_add_u32 v150, s74, 8, v123
	v_ashrrev_i32_e32 v123, 31, v122
	v_ashrrev_i32_e32 v124, 31, v150
	v_lshl_add_u64 v[122:123], v[122:123], 1, s[78:79]
	v_mul_lo_u32 v151, s70, v124
	v_mul_lo_u32 v146, s71, v150
	v_mad_u64_u32 v[124:125], s[78:79], s70, v150, 0
	v_add3_u32 v125, v125, v151, v146
	v_cvt_f32_i32_e32 v119, v119
	v_cvt_f32_i32_e32 v118, v118
	v_cvt_f32_i32_e32 v121, v121
	v_cvt_f32_i32_e32 v120, v120
	v_cvt_f32_i32_e32 v115, v115
	v_cvt_f32_i32_e32 v114, v114
	v_cvt_f32_i32_e32 v147, v117
	v_cvt_f32_i32_e32 v146, v116
	v_lshl_add_u64 v[124:125], v[124:125], 1, v[122:123]
	v_pk_mul_f32 v[116:117], v[118:119], s[58:59] op_sel_hi:[1,0]
	v_pk_mul_f32 v[118:119], v[120:121], s[58:59] op_sel_hi:[1,0]
	v_pk_mul_f32 v[120:121], v[114:115], s[58:59] op_sel_hi:[1,0]
	v_pk_mul_f32 v[146:147], v[146:147], s[58:59] op_sel_hi:[1,0]
	s_and_b64 vcc, exec, s[4:5]
	v_cvt_pk_bf16_f32 v126, v126, v127
	v_cvt_pk_bf16_f32 v127, v128, v129
	v_cvt_pk_bf16_f32 v128, v142, v143
	v_cvt_pk_bf16_f32 v129, v144, v145
	global_store_dwordx4 v[124:125], v[126:129], off nt
	s_cbranch_vccnz .LBB0_128
	v_mul_f32_e32 v114, 0xbfb8aa3b, v116
	v_exp_f32_e32 v114, v114
	v_mul_f32_e32 v115, 0xbfb8aa3b, v120
	v_exp_f32_e32 v115, v115
	v_add_f32_e32 v114, 1.0, v114
	v_rcp_f32_e32 v116, v114
	v_mul_f32_e32 v114, 0xbfb8aa3b, v117
	v_add_f32_e32 v115, 1.0, v115
	v_exp_f32_e32 v114, v114
	v_mul_f32_e32 v117, 0xbfb8aa3b, v121
	v_exp_f32_e32 v121, v117
	v_rcp_f32_e32 v120, v115
	v_mul_f32_e32 v115, 0xbfb8aa3b, v118
	v_exp_f32_e32 v115, v115
	v_mul_f32_e32 v118, 0xbfb8aa3b, v146
	v_add_f32_e32 v114, 1.0, v114
	v_exp_f32_e32 v126, v118
	v_rcp_f32_e32 v117, v114
	v_add_f32_e32 v114, 1.0, v121
	v_rcp_f32_e32 v121, v114
	v_add_f32_e32 v114, 1.0, v115
	v_mul_f32_e32 v115, 0xbfb8aa3b, v119
	v_exp_f32_e32 v115, v115
	v_mul_f32_e32 v119, 0xbfb8aa3b, v147
	v_rcp_f32_e32 v118, v114
	v_add_f32_e32 v114, 1.0, v126
	v_exp_f32_e32 v126, v119
	v_rcp_f32_e32 v146, v114
	v_add_f32_e32 v114, 1.0, v115
	v_rcp_f32_e32 v119, v114
	v_add_f32_e32 v114, 1.0, v126
	v_rcp_f32_e32 v147, v114
.LBB0_128:
	v_cvt_f32_i32_e32 v111, v111
	v_cvt_f32_i32_e32 v110, v110
	v_cvt_f32_i32_e32 v113, v113
	v_cvt_f32_i32_e32 v112, v112
	v_cvt_f32_i32_e32 v107, v107
	v_cvt_f32_i32_e32 v106, v106
	v_cvt_f32_i32_e32 v115, v109
	v_cvt_f32_i32_e32 v114, v108
	v_pk_mul_f32 v[108:109], v[110:111], s[58:59] op_sel_hi:[1,0]
	v_pk_mul_f32 v[110:111], v[112:113], s[58:59] op_sel_hi:[1,0]
	v_pk_mul_f32 v[112:113], v[106:107], s[58:59] op_sel_hi:[1,0]
	v_pk_mul_f32 v[114:115], v[114:115], s[58:59] op_sel_hi:[1,0]
	s_and_b64 vcc, exec, s[4:5]
	v_cvt_pk_bf16_f32 v116, v116, v117
	v_cvt_pk_bf16_f32 v117, v118, v119
	v_cvt_pk_bf16_f32 v118, v120, v121
	v_cvt_pk_bf16_f32 v119, v146, v147
	global_store_dwordx4 v[124:125], v[116:119], off offset:256 nt
	s_cbranch_vccnz .LBB0_130
	v_mul_f32_e32 v106, 0xbfb8aa3b, v108
	v_exp_f32_e32 v106, v106
	v_mul_f32_e32 v107, 0xbfb8aa3b, v112
	v_exp_f32_e32 v107, v107
	v_add_f32_e32 v106, 1.0, v106
	v_rcp_f32_e32 v108, v106
	v_mul_f32_e32 v106, 0xbfb8aa3b, v109
	v_add_f32_e32 v107, 1.0, v107
	v_exp_f32_e32 v106, v106
	v_mul_f32_e32 v109, 0xbfb8aa3b, v113
	v_exp_f32_e32 v113, v109
	v_rcp_f32_e32 v112, v107
	v_mul_f32_e32 v107, 0xbfb8aa3b, v110
	v_exp_f32_e32 v107, v107
	v_add_f32_e32 v106, 1.0, v106
	v_rcp_f32_e32 v109, v106
	v_add_f32_e32 v106, 1.0, v113
	v_mul_f32_e32 v110, 0xbfb8aa3b, v114
	v_exp_f32_e32 v114, v110
	v_rcp_f32_e32 v113, v106
	v_add_f32_e32 v106, 1.0, v107
	v_mul_f32_e32 v107, 0xbfb8aa3b, v111
	v_exp_f32_e32 v107, v107
	v_mul_f32_e32 v111, 0xbfb8aa3b, v115
	v_exp_f32_e32 v115, v111
	v_rcp_f32_e32 v110, v106
	v_add_f32_e32 v106, 1.0, v114
	v_rcp_f32_e32 v114, v106
	v_add_f32_e32 v106, 1.0, v107
	v_rcp_f32_e32 v111, v106
	v_add_f32_e32 v106, 1.0, v115
	v_rcp_f32_e32 v115, v106
.LBB0_130:
	v_or_b32_e32 v106, 16, v150
	v_mul_lo_u32 v116, s71, v106
	v_mad_u64_u32 v[106:107], s[78:79], s70, v106, 0
	v_add3_u32 v107, v107, v151, v116
	v_cvt_f32_i32_e32 v103, v103
	v_cvt_f32_i32_e32 v102, v102
	v_cvt_f32_i32_e32 v105, v105
	v_cvt_f32_i32_e32 v104, v104
	v_cvt_f32_i32_e32 v99, v99
	v_cvt_f32_i32_e32 v98, v98
	v_cvt_f32_i32_e32 v117, v101
	v_cvt_f32_i32_e32 v116, v100
	v_lshl_add_u64 v[106:107], v[106:107], 1, v[122:123]
	v_pk_mul_f32 v[100:101], v[102:103], s[58:59] op_sel_hi:[1,0]
	v_pk_mul_f32 v[102:103], v[104:105], s[58:59] op_sel_hi:[1,0]
	v_pk_mul_f32 v[104:105], v[98:99], s[58:59] op_sel_hi:[1,0]
	v_pk_mul_f32 v[116:117], v[116:117], s[58:59] op_sel_hi:[1,0]
	s_and_b64 vcc, exec, s[4:5]
	v_cvt_pk_bf16_f32 v108, v108, v109
	v_cvt_pk_bf16_f32 v109, v110, v111
	v_cvt_pk_bf16_f32 v110, v112, v113
	v_cvt_pk_bf16_f32 v111, v114, v115
	global_store_dwordx4 v[106:107], v[108:111], off nt
	s_cbranch_vccnz .LBB0_132
	v_mul_f32_e32 v98, 0xbfb8aa3b, v100
	v_exp_f32_e32 v98, v98
	v_mul_f32_e32 v99, 0xbfb8aa3b, v104
	v_exp_f32_e32 v99, v99
	v_add_f32_e32 v98, 1.0, v98
	v_rcp_f32_e32 v100, v98
	v_mul_f32_e32 v98, 0xbfb8aa3b, v101
	v_add_f32_e32 v99, 1.0, v99
	v_exp_f32_e32 v98, v98
	v_mul_f32_e32 v101, 0xbfb8aa3b, v105
	v_exp_f32_e32 v105, v101
	v_rcp_f32_e32 v104, v99
	v_mul_f32_e32 v99, 0xbfb8aa3b, v102
	v_exp_f32_e32 v99, v99
	v_mul_f32_e32 v102, 0xbfb8aa3b, v116
	v_add_f32_e32 v98, 1.0, v98
	v_exp_f32_e32 v108, v102
	v_rcp_f32_e32 v101, v98
	v_add_f32_e32 v98, 1.0, v105
	v_rcp_f32_e32 v105, v98
	v_add_f32_e32 v98, 1.0, v99
	v_mul_f32_e32 v99, 0xbfb8aa3b, v103
	v_exp_f32_e32 v99, v99
	v_mul_f32_e32 v103, 0xbfb8aa3b, v117
	v_rcp_f32_e32 v102, v98
	v_add_f32_e32 v98, 1.0, v108
	v_exp_f32_e32 v108, v103
	v_rcp_f32_e32 v116, v98
	v_add_f32_e32 v98, 1.0, v99
	v_rcp_f32_e32 v103, v98
	v_add_f32_e32 v98, 1.0, v108
	v_rcp_f32_e32 v117, v98
; __device__ __forceinline__ unsigned cvt_pk_bf16(float lo, float hi) { unsigned r; asm volatile("v_cvt_pk_bf16_f32 %0, %1, %2" : "=v"(r) : "v"(lo), "v"(hi)); return r; }
; __device__ __forceinline__ float fast_sigmoid(float x) { return __builtin_amdgcn_rcpf(1.0f + __builtin_amdgcn_exp2f(-1.44269504089f * x)); }
;     __device__ __forceinline__ void operator()(const f32x4 (&acc)[2][2][4][2], const Unit& u, int wr, int wc, int fr_, int fq_) const {
;     ...
;             for (int m = 0; m < 4; ++m) { bf16_t* rowp = base + (size_t)(row0 + ai * HALF + m * 16) * ldc + col0;
; #pragma unroll
;                 for (int bj = 0; bj < 2; ++bj) { f32x4 v0 = acc[ai][bj][m][0], v1 = acc[ai][bj][m][1];
;                     if (sig) {
; #pragma unroll
;                         for (int j = 0; j < 4; ++j) { v0[j] = fast_sigmoid(v0[j]); v1[j] = fast_sigmoid(v1[j]); } }
;                     u32x4 w; w.x = cvt_pk_bf16(v0[0], v0[1]); w.y = cvt_pk_bf16(v0[2], v0[3]); w.z = cvt_pk_bf16(v1[0], v1[1]); w.w = cvt_pk_bf16(v1[2], v1[3]);
;                     *(u32x4*)(rowp + bj * HALF) = w; } }
;     ...
;         if constexpr (F8 == 2) { const float dq_ = g.dq;
;             _Pragma("unroll") for (int a_ = 0; a_ < 2; ++a_) _Pragma("unroll") for (int b_ = 0; b_ < 2; ++b_) _Pragma("unroll") for (int m_ = 0; m_ < 4; ++m_) _Pragma("unroll") for (int n_ = 0; n_ < 2; ++n_) { const i32x4 c_ = __builtin_bit_cast(i32x4, acc[a_][b_][m_][n_]);
;                 acc[a_][b_][m_][n_] = (f32x4){(float)c_.x * dq_, (float)c_.y * dq_, (float)c_.z * dq_, (float)c_.w * dq_}; } }
.LBB0_132:
	v_cvt_f32_i32_e32 v95, v95
	v_cvt_f32_i32_e32 v94, v94
	v_cvt_f32_i32_e32 v97, v97
	v_cvt_f32_i32_e32 v96, v96
	v_cvt_f32_i32_e32 v91, v91
	v_cvt_f32_i32_e32 v90, v90
	v_cvt_f32_i32_e32 v99, v93
	v_cvt_f32_i32_e32 v98, v92
	v_pk_mul_f32 v[92:93], v[94:95], s[58:59] op_sel_hi:[1,0]
	v_pk_mul_f32 v[94:95], v[96:97], s[58:59] op_sel_hi:[1,0]
	v_pk_mul_f32 v[96:97], v[90:91], s[58:59] op_sel_hi:[1,0]
	v_pk_mul_f32 v[98:99], v[98:99], s[58:59] op_sel_hi:[1,0]
	s_and_b64 vcc, exec, s[4:5]
	v_cvt_pk_bf16_f32 v100, v100, v101
	v_cvt_pk_bf16_f32 v101, v102, v103
	v_cvt_pk_bf16_f32 v102, v104, v105
	v_cvt_pk_bf16_f32 v103, v116, v117
	global_store_dwordx4 v[106:107], v[100:103], off offset:256 nt
	s_cbranch_vccnz .LBB0_134
	v_mul_f32_e32 v90, 0xbfb8aa3b, v92
	v_exp_f32_e32 v90, v90
	v_mul_f32_e32 v91, 0xbfb8aa3b, v96
	v_exp_f32_e32 v91, v91
	v_add_f32_e32 v90, 1.0, v90
	v_rcp_f32_e32 v92, v90
	v_mul_f32_e32 v90, 0xbfb8aa3b, v93
	v_add_f32_e32 v91, 1.0, v91
	v_exp_f32_e32 v90, v90
	v_mul_f32_e32 v93, 0xbfb8aa3b, v97
	v_exp_f32_e32 v97, v93
	v_rcp_f32_e32 v96, v91
	v_mul_f32_e32 v91, 0xbfb8aa3b, v94
	v_exp_f32_e32 v91, v91
	v_add_f32_e32 v90, 1.0, v90
	v_rcp_f32_e32 v93, v90
	v_add_f32_e32 v90, 1.0, v97
	v_mul_f32_e32 v94, 0xbfb8aa3b, v98
	v_exp_f32_e32 v98, v94
	v_rcp_f32_e32 v97, v90
	v_add_f32_e32 v90, 1.0, v91
	v_mul_f32_e32 v91, 0xbfb8aa3b, v95
	v_exp_f32_e32 v91, v91
	v_mul_f32_e32 v95, 0xbfb8aa3b, v99
	v_exp_f32_e32 v99, v95
	v_rcp_f32_e32 v94, v90
	v_add_f32_e32 v90, 1.0, v98
	v_rcp_f32_e32 v98, v90
	v_add_f32_e32 v90, 1.0, v91
	v_rcp_f32_e32 v95, v90
	v_add_f32_e32 v90, 1.0, v99
	v_rcp_f32_e32 v99, v90
.LBB0_134:
	v_or_b32_e32 v90, 32, v150
	v_mul_lo_u32 v100, s71, v90
	v_mad_u64_u32 v[90:91], s[78:79], s70, v90, 0
	v_add3_u32 v91, v91, v151, v100
	v_cvt_f32_i32_e32 v87, v87
	v_cvt_f32_i32_e32 v86, v86
	v_cvt_f32_i32_e32 v89, v89
	v_cvt_f32_i32_e32 v88, v88
	v_cvt_f32_i32_e32 v83, v83
	v_cvt_f32_i32_e32 v82, v82
	v_cvt_f32_i32_e32 v101, v85
	v_cvt_f32_i32_e32 v100, v84
	v_lshl_add_u64 v[90:91], v[90:91], 1, v[122:123]
	v_pk_mul_f32 v[84:85], v[86:87], s[58:59] op_sel_hi:[1,0]
	v_pk_mul_f32 v[86:87], v[88:89], s[58:59] op_sel_hi:[1,0]
	v_pk_mul_f32 v[88:89], v[82:83], s[58:59] op_sel_hi:[1,0]
	v_pk_mul_f32 v[100:101], v[100:101], s[58:59] op_sel_hi:[1,0]
	s_and_b64 vcc, exec, s[4:5]
	v_cvt_pk_bf16_f32 v92, v92, v93
	v_cvt_pk_bf16_f32 v93, v94, v95
	v_cvt_pk_bf16_f32 v94, v96, v97
	v_cvt_pk_bf16_f32 v95, v98, v99
	global_store_dwordx4 v[90:91], v[92:95], off nt
	s_cbranch_vccnz .LBB0_136
	v_mul_f32_e32 v82, 0xbfb8aa3b, v84
	v_exp_f32_e32 v82, v82
	v_mul_f32_e32 v83, 0xbfb8aa3b, v88
	v_exp_f32_e32 v83, v83
	v_add_f32_e32 v82, 1.0, v82
	v_rcp_f32_e32 v84, v82
	v_mul_f32_e32 v82, 0xbfb8aa3b, v85
	v_add_f32_e32 v83, 1.0, v83
	v_exp_f32_e32 v82, v82
	v_mul_f32_e32 v85, 0xbfb8aa3b, v89
	v_exp_f32_e32 v89, v85
	v_rcp_f32_e32 v88, v83
	v_mul_f32_e32 v83, 0xbfb8aa3b, v86
	v_exp_f32_e32 v83, v83
	v_mul_f32_e32 v86, 0xbfb8aa3b, v100
	v_add_f32_e32 v82, 1.0, v82
	v_exp_f32_e32 v92, v86
	v_rcp_f32_e32 v85, v82
	v_add_f32_e32 v82, 1.0, v89
	v_rcp_f32_e32 v89, v82
	v_add_f32_e32 v82, 1.0, v83
	v_mul_f32_e32 v83, 0xbfb8aa3b, v87
	v_exp_f32_e32 v83, v83
	v_mul_f32_e32 v87, 0xbfb8aa3b, v101
	v_rcp_f32_e32 v86, v82
	v_add_f32_e32 v82, 1.0, v92
	v_exp_f32_e32 v92, v87
	v_rcp_f32_e32 v100, v82
	v_add_f32_e32 v82, 1.0, v83
	v_rcp_f32_e32 v87, v82
	v_add_f32_e32 v82, 1.0, v92
	v_rcp_f32_e32 v101, v82
.LBB0_136:
	v_cvt_f32_i32_e32 v79, v79
	v_cvt_f32_i32_e32 v78, v78
	v_cvt_f32_i32_e32 v81, v81
	v_cvt_f32_i32_e32 v80, v80
	v_cvt_f32_i32_e32 v75, v75
	v_cvt_f32_i32_e32 v74, v74
	v_cvt_f32_i32_e32 v83, v77
	v_cvt_f32_i32_e32 v82, v76
	v_pk_mul_f32 v[76:77], v[78:79], s[58:59] op_sel_hi:[1,0]
	v_pk_mul_f32 v[78:79], v[80:81], s[58:59] op_sel_hi:[1,0]
	v_pk_mul_f32 v[80:81], v[74:75], s[58:59] op_sel_hi:[1,0]
	v_pk_mul_f32 v[82:83], v[82:83], s[58:59] op_sel_hi:[1,0]
	s_and_b64 vcc, exec, s[4:5]
	v_cvt_pk_bf16_f32 v84, v84, v85
	v_cvt_pk_bf16_f32 v85, v86, v87
	v_cvt_pk_bf16_f32 v86, v88, v89
	v_cvt_pk_bf16_f32 v87, v100, v101
	global_store_dwordx4 v[90:91], v[84:87], off offset:256 nt
	s_cbranch_vccnz .LBB0_138
	v_mul_f32_e32 v74, 0xbfb8aa3b, v76
	v_exp_f32_e32 v74, v74
	v_mul_f32_e32 v75, 0xbfb8aa3b, v80
	v_exp_f32_e32 v75, v75
	v_add_f32_e32 v74, 1.0, v74
	v_rcp_f32_e32 v76, v74
	v_mul_f32_e32 v74, 0xbfb8aa3b, v77
	v_add_f32_e32 v75, 1.0, v75
	v_exp_f32_e32 v74, v74
	v_mul_f32_e32 v77, 0xbfb8aa3b, v81
	v_exp_f32_e32 v81, v77
	v_rcp_f32_e32 v80, v75
	v_mul_f32_e32 v75, 0xbfb8aa3b, v78
	v_exp_f32_e32 v75, v75
	v_add_f32_e32 v74, 1.0, v74
	v_rcp_f32_e32 v77, v74
	v_add_f32_e32 v74, 1.0, v81
	v_mul_f32_e32 v78, 0xbfb8aa3b, v82
	v_exp_f32_e32 v82, v78
	v_rcp_f32_e32 v81, v74
	v_add_f32_e32 v74, 1.0, v75
	v_mul_f32_e32 v75, 0xbfb8aa3b, v79
	v_exp_f32_e32 v75, v75
	v_mul_f32_e32 v79, 0xbfb8aa3b, v83
	v_exp_f32_e32 v83, v79
	v_rcp_f32_e32 v78, v74
	v_add_f32_e32 v74, 1.0, v82
	v_rcp_f32_e32 v82, v74
	v_add_f32_e32 v74, 1.0, v75
	v_rcp_f32_e32 v79, v74
	v_add_f32_e32 v74, 1.0, v83
	v_rcp_f32_e32 v83, v74
; __device__ __forceinline__ unsigned cvt_pk_bf16(float lo, float hi) { unsigned r; asm volatile("v_cvt_pk_bf16_f32 %0, %1, %2" : "=v"(r) : "v"(lo), "v"(hi)); return r; }
; __device__ __forceinline__ float fast_sigmoid(float x) { return __builtin_amdgcn_rcpf(1.0f + __builtin_amdgcn_exp2f(-1.44269504089f * x)); }
;     __device__ __forceinline__ void operator()(const f32x4 (&acc)[2][2][4][2], const Unit& u, int wr, int wc, int fr_, int fq_) const {
;     ...
;             for (int m = 0; m < 4; ++m) { bf16_t* rowp = base + (size_t)(row0 + ai * HALF + m * 16) * ldc + col0;
; #pragma unroll
;                 for (int bj = 0; bj < 2; ++bj) { f32x4 v0 = acc[ai][bj][m][0], v1 = acc[ai][bj][m][1];
;                     if (sig) {
; #pragma unroll
;                         for (int j = 0; j < 4; ++j) { v0[j] = fast_sigmoid(v0[j]); v1[j] = fast_sigmoid(v1[j]); } }
;                     u32x4 w; w.x = cvt_pk_bf16(v0[0], v0[1]); w.y = cvt_pk_bf16(v0[2], v0[3]); w.z = cvt_pk_bf16(v1[0], v1[1]); w.w = cvt_pk_bf16(v1[2], v1[3]);
;                     *(u32x4*)(rowp + bj * HALF) = w; } }
;     ...
;         if constexpr (F8 == 2) { const float dq_ = g.dq;
;             _Pragma("unroll") for (int a_ = 0; a_ < 2; ++a_) _Pragma("unroll") for (int b_ = 0; b_ < 2; ++b_) _Pragma("unroll") for (int m_ = 0; m_ < 4; ++m_) _Pragma("unroll") for (int n_ = 0; n_ < 2; ++n_) { const i32x4 c_ = __builtin_bit_cast(i32x4, acc[a_][b_][m_][n_]);
;                 acc[a_][b_][m_][n_] = (f32x4){(float)c_.x * dq_, (float)c_.y * dq_, (float)c_.z * dq_, (float)c_.w * dq_}; } }
.LBB0_138:
	v_or_b32_e32 v74, 48, v150
	v_mul_lo_u32 v84, s71, v74
	v_mad_u64_u32 v[74:75], s[78:79], s70, v74, 0
	v_add3_u32 v75, v75, v151, v84
	v_cvt_f32_i32_e32 v71, v71
	v_cvt_f32_i32_e32 v70, v70
	v_cvt_f32_i32_e32 v73, v73
	v_cvt_f32_i32_e32 v72, v72
	v_cvt_f32_i32_e32 v67, v67
	v_cvt_f32_i32_e32 v66, v66
	v_cvt_f32_i32_e32 v85, v69
	v_cvt_f32_i32_e32 v84, v68
	v_lshl_add_u64 v[74:75], v[74:75], 1, v[122:123]
	v_pk_mul_f32 v[68:69], v[70:71], s[58:59] op_sel_hi:[1,0]
	v_pk_mul_f32 v[70:71], v[72:73], s[58:59] op_sel_hi:[1,0]
	v_pk_mul_f32 v[72:73], v[66:67], s[58:59] op_sel_hi:[1,0]
	v_pk_mul_f32 v[84:85], v[84:85], s[58:59] op_sel_hi:[1,0]
	s_and_b64 vcc, exec, s[4:5]
	v_cvt_pk_bf16_f32 v76, v76, v77
	v_cvt_pk_bf16_f32 v77, v78, v79
	v_cvt_pk_bf16_f32 v78, v80, v81
	v_cvt_pk_bf16_f32 v79, v82, v83
	global_store_dwordx4 v[74:75], v[76:79], off nt
	s_cbranch_vccnz .LBB0_140
	v_mul_f32_e32 v66, 0xbfb8aa3b, v68
	v_exp_f32_e32 v66, v66
	v_mul_f32_e32 v67, 0xbfb8aa3b, v72
	v_exp_f32_e32 v67, v67
	v_add_f32_e32 v66, 1.0, v66
	v_rcp_f32_e32 v68, v66
	v_mul_f32_e32 v66, 0xbfb8aa3b, v69
	v_add_f32_e32 v67, 1.0, v67
	v_exp_f32_e32 v66, v66
	v_mul_f32_e32 v69, 0xbfb8aa3b, v73
	v_exp_f32_e32 v73, v69
	v_rcp_f32_e32 v72, v67
	v_mul_f32_e32 v67, 0xbfb8aa3b, v70
	v_exp_f32_e32 v67, v67
	v_mul_f32_e32 v70, 0xbfb8aa3b, v84
	v_add_f32_e32 v66, 1.0, v66
	v_exp_f32_e32 v76, v70
	v_rcp_f32_e32 v69, v66
	v_add_f32_e32 v66, 1.0, v73
	v_rcp_f32_e32 v73, v66
	v_add_f32_e32 v66, 1.0, v67
	v_mul_f32_e32 v67, 0xbfb8aa3b, v71
	v_exp_f32_e32 v67, v67
	v_mul_f32_e32 v71, 0xbfb8aa3b, v85
	v_rcp_f32_e32 v70, v66
	v_add_f32_e32 v66, 1.0, v76
	v_exp_f32_e32 v76, v71
	v_rcp_f32_e32 v84, v66
	v_add_f32_e32 v66, 1.0, v67
	v_rcp_f32_e32 v71, v66
	v_add_f32_e32 v66, 1.0, v76
	v_rcp_f32_e32 v85, v66
.LBB0_140:
	v_cvt_f32_i32_e32 v63, v63
	v_cvt_f32_i32_e32 v62, v62
	v_cvt_f32_i32_e32 v65, v65
	v_cvt_f32_i32_e32 v64, v64
	v_cvt_f32_i32_e32 v59, v59
	v_cvt_f32_i32_e32 v58, v58
	v_cvt_f32_i32_e32 v67, v61
	v_cvt_f32_i32_e32 v66, v60
	v_pk_mul_f32 v[60:61], v[62:63], s[58:59] op_sel_hi:[1,0]
	v_pk_mul_f32 v[62:63], v[64:65], s[58:59] op_sel_hi:[1,0]
	v_pk_mul_f32 v[64:65], v[58:59], s[58:59] op_sel_hi:[1,0]
	v_pk_mul_f32 v[66:67], v[66:67], s[58:59] op_sel_hi:[1,0]
	s_and_b64 vcc, exec, s[4:5]
	v_cvt_pk_bf16_f32 v68, v68, v69
	v_cvt_pk_bf16_f32 v69, v70, v71
	v_cvt_pk_bf16_f32 v70, v72, v73
	v_cvt_pk_bf16_f32 v71, v84, v85
	global_store_dwordx4 v[74:75], v[68:71], off offset:256 nt
	s_cbranch_vccnz .LBB0_142
	v_mul_f32_e32 v58, 0xbfb8aa3b, v60
	v_exp_f32_e32 v58, v58
	v_mul_f32_e32 v59, 0xbfb8aa3b, v64
	v_exp_f32_e32 v59, v59
	v_add_f32_e32 v58, 1.0, v58
	v_rcp_f32_e32 v60, v58
	v_mul_f32_e32 v58, 0xbfb8aa3b, v61
	v_add_f32_e32 v59, 1.0, v59
	v_exp_f32_e32 v58, v58
	v_mul_f32_e32 v61, 0xbfb8aa3b, v65
	v_exp_f32_e32 v65, v61
	v_rcp_f32_e32 v64, v59
	v_mul_f32_e32 v59, 0xbfb8aa3b, v62
	v_exp_f32_e32 v59, v59
	v_add_f32_e32 v58, 1.0, v58
	v_rcp_f32_e32 v61, v58
	v_add_f32_e32 v58, 1.0, v65
	v_mul_f32_e32 v62, 0xbfb8aa3b, v66
	v_exp_f32_e32 v66, v62
	v_rcp_f32_e32 v65, v58
	v_add_f32_e32 v58, 1.0, v59
	v_mul_f32_e32 v59, 0xbfb8aa3b, v63
	v_exp_f32_e32 v59, v59
	v_mul_f32_e32 v63, 0xbfb8aa3b, v67
	v_exp_f32_e32 v67, v63
	v_rcp_f32_e32 v62, v58
	v_add_f32_e32 v58, 1.0, v66
	v_rcp_f32_e32 v66, v58
	v_add_f32_e32 v58, 1.0, v59
	v_rcp_f32_e32 v63, v58
	v_add_f32_e32 v58, 1.0, v67
	v_rcp_f32_e32 v67, v58
.LBB0_142:
	v_add_u32_e32 v58, 0x80, v150
	v_ashrrev_i32_e32 v59, 31, v58
	v_mul_lo_u32 v68, s70, v59
	v_mul_lo_u32 v69, s71, v58
	v_mad_u64_u32 v[58:59], s[78:79], s70, v58, 0
	v_add3_u32 v59, v59, v68, v69
	v_cvt_f32_i32_e32 v55, v55
	v_cvt_f32_i32_e32 v54, v54
	v_cvt_f32_i32_e32 v57, v57
	v_cvt_f32_i32_e32 v56, v56
	v_cvt_f32_i32_e32 v51, v51
	v_cvt_f32_i32_e32 v50, v50
	v_cvt_f32_i32_e32 v69, v53
	v_cvt_f32_i32_e32 v68, v52
	v_lshl_add_u64 v[58:59], v[58:59], 1, v[122:123]
	v_pk_mul_f32 v[52:53], v[54:55], s[58:59] op_sel_hi:[1,0]
	v_pk_mul_f32 v[54:55], v[56:57], s[58:59] op_sel_hi:[1,0]
	v_pk_mul_f32 v[56:57], v[50:51], s[58:59] op_sel_hi:[1,0]
	v_pk_mul_f32 v[68:69], v[68:69], s[58:59] op_sel_hi:[1,0]
	s_and_b64 vcc, exec, s[4:5]
	v_cvt_pk_bf16_f32 v60, v60, v61
	v_cvt_pk_bf16_f32 v61, v62, v63
	v_cvt_pk_bf16_f32 v62, v64, v65
	v_cvt_pk_bf16_f32 v63, v66, v67
	global_store_dwordx4 v[58:59], v[60:63], off nt
	s_cbranch_vccnz .LBB0_144
	v_mul_f32_e32 v50, 0xbfb8aa3b, v52
	v_exp_f32_e32 v50, v50
	v_mul_f32_e32 v51, 0xbfb8aa3b, v56
	v_exp_f32_e32 v51, v51
	v_add_f32_e32 v50, 1.0, v50
	v_rcp_f32_e32 v52, v50
	v_mul_f32_e32 v50, 0xbfb8aa3b, v53
	v_add_f32_e32 v51, 1.0, v51
	v_exp_f32_e32 v50, v50
	v_mul_f32_e32 v53, 0xbfb8aa3b, v57
	v_exp_f32_e32 v57, v53
	v_rcp_f32_e32 v56, v51
	v_mul_f32_e32 v51, 0xbfb8aa3b, v54
	v_exp_f32_e32 v51, v51
	v_mul_f32_e32 v54, 0xbfb8aa3b, v68
	v_add_f32_e32 v50, 1.0, v50
	v_exp_f32_e32 v60, v54
	v_rcp_f32_e32 v53, v50
	v_add_f32_e32 v50, 1.0, v57
	v_rcp_f32_e32 v57, v50
	v_add_f32_e32 v50, 1.0, v51
	v_mul_f32_e32 v51, 0xbfb8aa3b, v55
	v_exp_f32_e32 v51, v51
	v_mul_f32_e32 v55, 0xbfb8aa3b, v69
	v_rcp_f32_e32 v54, v50
	v_add_f32_e32 v50, 1.0, v60
	v_exp_f32_e32 v60, v55
	v_rcp_f32_e32 v68, v50
	v_add_f32_e32 v50, 1.0, v51
	v_rcp_f32_e32 v55, v50
	v_add_f32_e32 v50, 1.0, v60
	v_rcp_f32_e32 v69, v50
; __device__ __forceinline__ unsigned cvt_pk_bf16(float lo, float hi) { unsigned r; asm volatile("v_cvt_pk_bf16_f32 %0, %1, %2" : "=v"(r) : "v"(lo), "v"(hi)); return r; }
; __device__ __forceinline__ float fast_sigmoid(float x) { return __builtin_amdgcn_rcpf(1.0f + __builtin_amdgcn_exp2f(-1.44269504089f * x)); }
;     __device__ __forceinline__ void operator()(const f32x4 (&acc)[2][2][4][2], const Unit& u, int wr, int wc, int fr_, int fq_) const {
;     ...
;             for (int m = 0; m < 4; ++m) { bf16_t* rowp = base + (size_t)(row0 + ai * HALF + m * 16) * ldc + col0;
; #pragma unroll
;                 for (int bj = 0; bj < 2; ++bj) { f32x4 v0 = acc[ai][bj][m][0], v1 = acc[ai][bj][m][1];
;                     if (sig) {
; #pragma unroll
;                         for (int j = 0; j < 4; ++j) { v0[j] = fast_sigmoid(v0[j]); v1[j] = fast_sigmoid(v1[j]); } }
;                     u32x4 w; w.x = cvt_pk_bf16(v0[0], v0[1]); w.y = cvt_pk_bf16(v0[2], v0[3]); w.z = cvt_pk_bf16(v1[0], v1[1]); w.w = cvt_pk_bf16(v1[2], v1[3]);
;                     *(u32x4*)(rowp + bj * HALF) = w; } }
;     ...
;         if constexpr (F8 == 2) { const float dq_ = g.dq;
;             _Pragma("unroll") for (int a_ = 0; a_ < 2; ++a_) _Pragma("unroll") for (int b_ = 0; b_ < 2; ++b_) _Pragma("unroll") for (int m_ = 0; m_ < 4; ++m_) _Pragma("unroll") for (int n_ = 0; n_ < 2; ++n_) { const i32x4 c_ = __builtin_bit_cast(i32x4, acc[a_][b_][m_][n_]);
;                 acc[a_][b_][m_][n_] = (f32x4){(float)c_.x * dq_, (float)c_.y * dq_, (float)c_.z * dq_, (float)c_.w * dq_}; } }
.LBB0_144:
	v_cvt_f32_i32_e32 v47, v47
	v_cvt_f32_i32_e32 v46, v46
	v_cvt_f32_i32_e32 v49, v49
	v_cvt_f32_i32_e32 v48, v48
	v_cvt_f32_i32_e32 v43, v43
	v_cvt_f32_i32_e32 v42, v42
	v_cvt_f32_i32_e32 v51, v45
	v_cvt_f32_i32_e32 v50, v44
	v_pk_mul_f32 v[44:45], v[46:47], s[58:59] op_sel_hi:[1,0]
	v_pk_mul_f32 v[46:47], v[48:49], s[58:59] op_sel_hi:[1,0]
	v_pk_mul_f32 v[48:49], v[42:43], s[58:59] op_sel_hi:[1,0]
	v_pk_mul_f32 v[50:51], v[50:51], s[58:59] op_sel_hi:[1,0]
	s_and_b64 vcc, exec, s[4:5]
	v_cvt_pk_bf16_f32 v52, v52, v53
	v_cvt_pk_bf16_f32 v53, v54, v55
	v_cvt_pk_bf16_f32 v54, v56, v57
	v_cvt_pk_bf16_f32 v55, v68, v69
	global_store_dwordx4 v[58:59], v[52:55], off offset:256 nt
	s_cbranch_vccnz .LBB0_146
	v_mul_f32_e32 v42, 0xbfb8aa3b, v44
	v_exp_f32_e32 v42, v42
	v_mul_f32_e32 v43, 0xbfb8aa3b, v48
	v_exp_f32_e32 v43, v43
	v_add_f32_e32 v42, 1.0, v42
	v_rcp_f32_e32 v44, v42
	v_mul_f32_e32 v42, 0xbfb8aa3b, v45
	v_add_f32_e32 v43, 1.0, v43
	v_exp_f32_e32 v42, v42
	v_mul_f32_e32 v45, 0xbfb8aa3b, v49
	v_exp_f32_e32 v49, v45
	v_rcp_f32_e32 v48, v43
	v_mul_f32_e32 v43, 0xbfb8aa3b, v46
	v_exp_f32_e32 v43, v43
	v_add_f32_e32 v42, 1.0, v42
	v_rcp_f32_e32 v45, v42
	v_add_f32_e32 v42, 1.0, v49
	v_mul_f32_e32 v46, 0xbfb8aa3b, v50
	v_exp_f32_e32 v50, v46
	v_rcp_f32_e32 v49, v42
	v_add_f32_e32 v42, 1.0, v43
	v_mul_f32_e32 v43, 0xbfb8aa3b, v47
	v_exp_f32_e32 v43, v43
	v_mul_f32_e32 v47, 0xbfb8aa3b, v51
	v_exp_f32_e32 v51, v47
	v_rcp_f32_e32 v46, v42
	v_add_f32_e32 v42, 1.0, v50
	v_rcp_f32_e32 v50, v42
	v_add_f32_e32 v42, 1.0, v43
	v_rcp_f32_e32 v47, v42
	v_add_f32_e32 v42, 1.0, v51
	v_rcp_f32_e32 v51, v42
.LBB0_146:
	v_add_u32_e32 v42, 0x90, v150
	v_ashrrev_i32_e32 v43, 31, v42
	v_mul_lo_u32 v52, s70, v43
	v_mul_lo_u32 v53, s71, v42
	v_mad_u64_u32 v[42:43], s[78:79], s70, v42, 0
	v_add3_u32 v43, v43, v52, v53
	v_cvt_f32_i32_e32 v39, v39
	v_cvt_f32_i32_e32 v38, v38
	v_cvt_f32_i32_e32 v41, v41
	v_cvt_f32_i32_e32 v40, v40
	v_cvt_f32_i32_e32 v35, v35
	v_cvt_f32_i32_e32 v34, v34
	v_cvt_f32_i32_e32 v53, v37
	v_cvt_f32_i32_e32 v52, v36
	v_lshl_add_u64 v[42:43], v[42:43], 1, v[122:123]
	v_pk_mul_f32 v[36:37], v[38:39], s[58:59] op_sel_hi:[1,0]
	v_pk_mul_f32 v[38:39], v[40:41], s[58:59] op_sel_hi:[1,0]
	v_pk_mul_f32 v[40:41], v[34:35], s[58:59] op_sel_hi:[1,0]
	v_pk_mul_f32 v[52:53], v[52:53], s[58:59] op_sel_hi:[1,0]
	s_and_b64 vcc, exec, s[4:5]
	v_cvt_pk_bf16_f32 v44, v44, v45
	v_cvt_pk_bf16_f32 v45, v46, v47
	v_cvt_pk_bf16_f32 v46, v48, v49
	v_cvt_pk_bf16_f32 v47, v50, v51
	global_store_dwordx4 v[42:43], v[44:47], off nt
	s_cbranch_vccnz .LBB0_148
	v_mul_f32_e32 v34, 0xbfb8aa3b, v36
	v_exp_f32_e32 v34, v34
	v_mul_f32_e32 v35, 0xbfb8aa3b, v40
	v_exp_f32_e32 v35, v35
	v_add_f32_e32 v34, 1.0, v34
	v_rcp_f32_e32 v36, v34
	v_mul_f32_e32 v34, 0xbfb8aa3b, v37
	v_add_f32_e32 v35, 1.0, v35
	v_exp_f32_e32 v34, v34
	v_mul_f32_e32 v37, 0xbfb8aa3b, v41
	v_exp_f32_e32 v41, v37
	v_rcp_f32_e32 v40, v35
	v_mul_f32_e32 v35, 0xbfb8aa3b, v38
	v_exp_f32_e32 v35, v35
	v_mul_f32_e32 v38, 0xbfb8aa3b, v52
	v_add_f32_e32 v34, 1.0, v34
	v_exp_f32_e32 v44, v38
	v_rcp_f32_e32 v37, v34
	v_add_f32_e32 v34, 1.0, v41
	v_rcp_f32_e32 v41, v34
	v_add_f32_e32 v34, 1.0, v35
	v_mul_f32_e32 v35, 0xbfb8aa3b, v39
	v_exp_f32_e32 v35, v35
	v_mul_f32_e32 v39, 0xbfb8aa3b, v53
	v_rcp_f32_e32 v38, v34
	v_add_f32_e32 v34, 1.0, v44
	v_exp_f32_e32 v44, v39
	v_rcp_f32_e32 v52, v34
	v_add_f32_e32 v34, 1.0, v35
	v_rcp_f32_e32 v39, v34
	v_add_f32_e32 v34, 1.0, v44
	v_rcp_f32_e32 v53, v34
.LBB0_148:
	v_cvt_f32_i32_e32 v31, v31
	v_cvt_f32_i32_e32 v30, v30
	v_cvt_f32_i32_e32 v33, v33
	v_cvt_f32_i32_e32 v32, v32
	v_cvt_f32_i32_e32 v27, v27
	v_cvt_f32_i32_e32 v26, v26
	v_cvt_f32_i32_e32 v35, v29
	v_cvt_f32_i32_e32 v34, v28
	v_pk_mul_f32 v[28:29], v[30:31], s[58:59] op_sel_hi:[1,0]
	v_pk_mul_f32 v[30:31], v[32:33], s[58:59] op_sel_hi:[1,0]
	v_pk_mul_f32 v[32:33], v[26:27], s[58:59] op_sel_hi:[1,0]
	v_pk_mul_f32 v[34:35], v[34:35], s[58:59] op_sel_hi:[1,0]
	s_and_b64 vcc, exec, s[4:5]
	v_cvt_pk_bf16_f32 v36, v36, v37
	v_cvt_pk_bf16_f32 v37, v38, v39
	v_cvt_pk_bf16_f32 v38, v40, v41
	v_cvt_pk_bf16_f32 v39, v52, v53
	global_store_dwordx4 v[42:43], v[36:39], off offset:256 nt
	s_cbranch_vccnz .LBB0_150
	v_mul_f32_e32 v26, 0xbfb8aa3b, v28
	v_exp_f32_e32 v26, v26
	v_mul_f32_e32 v27, 0xbfb8aa3b, v32
	v_exp_f32_e32 v27, v27
	v_add_f32_e32 v26, 1.0, v26
	v_rcp_f32_e32 v28, v26
	v_mul_f32_e32 v26, 0xbfb8aa3b, v29
	v_add_f32_e32 v27, 1.0, v27
	v_exp_f32_e32 v26, v26
	v_mul_f32_e32 v29, 0xbfb8aa3b, v33
	v_exp_f32_e32 v33, v29
	v_rcp_f32_e32 v32, v27
	v_mul_f32_e32 v27, 0xbfb8aa3b, v30
	v_exp_f32_e32 v27, v27
	v_add_f32_e32 v26, 1.0, v26
	v_rcp_f32_e32 v29, v26
	v_add_f32_e32 v26, 1.0, v33
	v_mul_f32_e32 v30, 0xbfb8aa3b, v34
	v_exp_f32_e32 v34, v30
	v_rcp_f32_e32 v33, v26
	v_add_f32_e32 v26, 1.0, v27
	v_mul_f32_e32 v27, 0xbfb8aa3b, v31
	v_exp_f32_e32 v27, v27
	v_mul_f32_e32 v31, 0xbfb8aa3b, v35
	v_exp_f32_e32 v35, v31
	v_rcp_f32_e32 v30, v26
	v_add_f32_e32 v26, 1.0, v34
	v_rcp_f32_e32 v34, v26
	v_add_f32_e32 v26, 1.0, v27
	v_rcp_f32_e32 v31, v26
	v_add_f32_e32 v26, 1.0, v35
	v_rcp_f32_e32 v35, v26
; __device__ __forceinline__ unsigned cvt_pk_bf16(float lo, float hi) { unsigned r; asm volatile("v_cvt_pk_bf16_f32 %0, %1, %2" : "=v"(r) : "v"(lo), "v"(hi)); return r; }
; __device__ __forceinline__ float fast_sigmoid(float x) { return __builtin_amdgcn_rcpf(1.0f + __builtin_amdgcn_exp2f(-1.44269504089f * x)); }
; #define PG8_BAR __builtin_amdgcn_s_barrier()
;     __device__ __forceinline__ void operator()(const f32x4 (&acc)[2][2][4][2], const Unit& u, int wr, int wc, int fr_, int fq_) const {
;     ...
;             for (int m = 0; m < 4; ++m) { bf16_t* rowp = base + (size_t)(row0 + ai * HALF + m * 16) * ldc + col0;
; #pragma unroll
;                 for (int bj = 0; bj < 2; ++bj) { f32x4 v0 = acc[ai][bj][m][0], v1 = acc[ai][bj][m][1];
;                     if (sig) {
; #pragma unroll
;                         for (int j = 0; j < 4; ++j) { v0[j] = fast_sigmoid(v0[j]); v1[j] = fast_sigmoid(v1[j]); } }
;                     u32x4 w; w.x = cvt_pk_bf16(v0[0], v0[1]); w.y = cvt_pk_bf16(v0[2], v0[3]); w.z = cvt_pk_bf16(v1[0], v1[1]); w.w = cvt_pk_bf16(v1[2], v1[3]);
;                     *(u32x4*)(rowp + bj * HALF) = w; } }
;     ...
;         if (!has_next) break;
; #pragma unroll
;         for (int a = 0; a < 2; ++a)
; #pragma unroll
;             for (int b = 0; b < 2; ++b)
; #pragma unroll
;                 for (int m = 0; m < 4; ++m)
; #pragma unroll
;                     for (int n = 0; n < 2; ++n) acc[a][b][m][n] = (f32x4){0.f, 0.f, 0.f, 0.f};
;         cur = nxt; cA = nA; cB = nB; ++ui;
;         if constexpr (ALIGN_EPI) { if (wr == 1) PG8_BAR; }
.LBB0_150:
	v_add_u32_e32 v26, 0xa0, v150
	v_ashrrev_i32_e32 v27, 31, v26
	v_mul_lo_u32 v36, s70, v27
	v_mul_lo_u32 v37, s71, v26
	v_mad_u64_u32 v[26:27], s[78:79], s70, v26, 0
	v_add3_u32 v27, v27, v36, v37
	v_cvt_f32_i32_e32 v23, v23
	v_cvt_f32_i32_e32 v22, v22
	v_cvt_f32_i32_e32 v25, v25
	v_cvt_f32_i32_e32 v24, v24
	v_cvt_f32_i32_e32 v37, v19
	v_cvt_f32_i32_e32 v36, v18
	v_cvt_f32_i32_e32 v39, v21
	v_cvt_f32_i32_e32 v38, v20
	v_lshl_add_u64 v[26:27], v[26:27], 1, v[122:123]
	v_pk_mul_f32 v[18:19], v[22:23], s[58:59] op_sel_hi:[1,0]
	v_pk_mul_f32 v[20:21], v[24:25], s[58:59] op_sel_hi:[1,0]
	v_pk_mul_f32 v[22:23], v[36:37], s[58:59] op_sel_hi:[1,0]
	v_pk_mul_f32 v[24:25], v[38:39], s[58:59] op_sel_hi:[1,0]
	s_and_b64 vcc, exec, s[4:5]
	v_cvt_pk_bf16_f32 v28, v28, v29
	v_cvt_pk_bf16_f32 v29, v30, v31
	v_cvt_pk_bf16_f32 v30, v32, v33
	v_cvt_pk_bf16_f32 v31, v34, v35
	global_store_dwordx4 v[26:27], v[28:31], off nt
	s_cbranch_vccnz .LBB0_152
	v_mul_f32_e32 v18, 0xbfb8aa3b, v18
	v_mul_f32_e32 v22, 0xbfb8aa3b, v22
	v_mul_f32_e32 v19, 0xbfb8aa3b, v19
	v_mul_f32_e32 v23, 0xbfb8aa3b, v23
	v_mul_f32_e32 v20, 0xbfb8aa3b, v20
	v_mul_f32_e32 v24, 0xbfb8aa3b, v24
	v_mul_f32_e32 v21, 0xbfb8aa3b, v21
	v_mul_f32_e32 v25, 0xbfb8aa3b, v25
	v_exp_f32_e32 v18, v18
	v_exp_f32_e32 v22, v22
	v_exp_f32_e32 v19, v19
	v_exp_f32_e32 v23, v23
	v_exp_f32_e32 v20, v20
	v_exp_f32_e32 v24, v24
	v_exp_f32_e32 v21, v21
	v_exp_f32_e32 v25, v25
	v_add_f32_e32 v18, 1.0, v18
	v_add_f32_e32 v22, 1.0, v22
	v_add_f32_e32 v19, 1.0, v19
	v_add_f32_e32 v23, 1.0, v23
	v_add_f32_e32 v20, 1.0, v20
	v_add_f32_e32 v24, 1.0, v24
	v_add_f32_e32 v21, 1.0, v21
	v_add_f32_e32 v25, 1.0, v25
	v_rcp_f32_e32 v18, v18
	v_rcp_f32_e32 v22, v22
	v_rcp_f32_e32 v19, v19
	v_rcp_f32_e32 v23, v23
	v_rcp_f32_e32 v20, v20
	v_rcp_f32_e32 v24, v24
	v_rcp_f32_e32 v21, v21
	v_rcp_f32_e32 v25, v25
.LBB0_152:
	v_cvt_f32_i32_e32 v15, v15
	v_cvt_f32_i32_e32 v14, v14
	v_cvt_f32_i32_e32 v17, v17
	v_cvt_f32_i32_e32 v16, v16
	v_cvt_f32_i32_e32 v29, v11
	v_cvt_f32_i32_e32 v28, v10
	v_cvt_f32_i32_e32 v31, v13
	v_cvt_f32_i32_e32 v30, v12
	v_pk_mul_f32 v[10:11], v[14:15], s[58:59] op_sel_hi:[1,0]
	v_pk_mul_f32 v[12:13], v[16:17], s[58:59] op_sel_hi:[1,0]
	v_pk_mul_f32 v[14:15], v[28:29], s[58:59] op_sel_hi:[1,0]
	v_pk_mul_f32 v[16:17], v[30:31], s[58:59] op_sel_hi:[1,0]
	s_and_b64 vcc, exec, s[4:5]
	v_cvt_pk_bf16_f32 v18, v18, v19
	v_cvt_pk_bf16_f32 v19, v20, v21
	v_cvt_pk_bf16_f32 v20, v22, v23
	v_cvt_pk_bf16_f32 v21, v24, v25
	global_store_dwordx4 v[26:27], v[18:21], off offset:256 nt
	s_cbranch_vccnz .LBB0_154
	v_mul_f32_e32 v10, 0xbfb8aa3b, v10
	v_mul_f32_e32 v14, 0xbfb8aa3b, v14
	v_mul_f32_e32 v11, 0xbfb8aa3b, v11
	v_mul_f32_e32 v15, 0xbfb8aa3b, v15
	v_mul_f32_e32 v12, 0xbfb8aa3b, v12
	v_mul_f32_e32 v16, 0xbfb8aa3b, v16
	v_mul_f32_e32 v13, 0xbfb8aa3b, v13
	v_mul_f32_e32 v17, 0xbfb8aa3b, v17
	v_exp_f32_e32 v10, v10
	v_exp_f32_e32 v14, v14
	v_exp_f32_e32 v11, v11
	v_exp_f32_e32 v15, v15
	v_exp_f32_e32 v12, v12
	v_exp_f32_e32 v16, v16
	v_exp_f32_e32 v13, v13
	v_exp_f32_e32 v17, v17
	v_add_f32_e32 v10, 1.0, v10
	v_add_f32_e32 v14, 1.0, v14
	v_add_f32_e32 v11, 1.0, v11
	v_add_f32_e32 v15, 1.0, v15
	v_add_f32_e32 v12, 1.0, v12
	v_add_f32_e32 v16, 1.0, v16
	v_add_f32_e32 v13, 1.0, v13
	v_add_f32_e32 v17, 1.0, v17
	v_rcp_f32_e32 v10, v10
	v_rcp_f32_e32 v14, v14
	v_rcp_f32_e32 v11, v11
	v_rcp_f32_e32 v15, v15
	v_rcp_f32_e32 v12, v12
	v_rcp_f32_e32 v16, v16
	v_rcp_f32_e32 v13, v13
	v_rcp_f32_e32 v17, v17
.LBB0_154:
	s_nop 0
	v_add_u32_e32 v18, 0xb0, v150
	v_ashrrev_i32_e32 v19, 31, v18
	v_mul_lo_u32 v20, s70, v19
	v_mul_lo_u32 v21, s71, v18
	v_mad_u64_u32 v[18:19], s[70:71], s70, v18, 0
	v_add3_u32 v19, v19, v20, v21
	v_cvt_f32_i32_e32 v7, v7
	v_cvt_f32_i32_e32 v6, v6
	v_cvt_f32_i32_e32 v9, v9
	v_cvt_f32_i32_e32 v8, v8
	v_cvt_f32_i32_e32 v21, v3
	v_cvt_f32_i32_e32 v20, v2
	v_cvt_f32_i32_e32 v23, v5
	v_cvt_f32_i32_e32 v22, v4
	v_lshl_add_u64 v[18:19], v[18:19], 1, v[122:123]
	v_pk_mul_f32 v[2:3], v[6:7], s[58:59] op_sel_hi:[1,0]
	v_pk_mul_f32 v[4:5], v[8:9], s[58:59] op_sel_hi:[1,0]
	v_pk_mul_f32 v[6:7], v[20:21], s[58:59] op_sel_hi:[1,0]
	v_pk_mul_f32 v[8:9], v[22:23], s[58:59] op_sel_hi:[1,0]
	s_and_b64 vcc, exec, s[4:5]
	v_cvt_pk_bf16_f32 v10, v10, v11
	v_cvt_pk_bf16_f32 v11, v12, v13
	v_cvt_pk_bf16_f32 v12, v14, v15
	v_cvt_pk_bf16_f32 v13, v16, v17
	global_store_dwordx4 v[18:19], v[10:13], off nt
	s_cbranch_vccnz .LBB0_156
	v_mul_f32_e32 v2, 0xbfb8aa3b, v2
	v_mul_f32_e32 v6, 0xbfb8aa3b, v6
	v_mul_f32_e32 v3, 0xbfb8aa3b, v3
	v_mul_f32_e32 v7, 0xbfb8aa3b, v7
	v_mul_f32_e32 v4, 0xbfb8aa3b, v4
	v_mul_f32_e32 v8, 0xbfb8aa3b, v8
	v_mul_f32_e32 v5, 0xbfb8aa3b, v5
	v_mul_f32_e32 v9, 0xbfb8aa3b, v9
	v_exp_f32_e32 v2, v2
	v_exp_f32_e32 v6, v6
	v_exp_f32_e32 v3, v3
	v_exp_f32_e32 v7, v7
	v_exp_f32_e32 v4, v4
	v_exp_f32_e32 v8, v8
	v_exp_f32_e32 v5, v5
	v_exp_f32_e32 v9, v9
	v_add_f32_e32 v2, 1.0, v2
	v_add_f32_e32 v6, 1.0, v6
	v_add_f32_e32 v3, 1.0, v3
	v_add_f32_e32 v7, 1.0, v7
	v_add_f32_e32 v4, 1.0, v4
	v_add_f32_e32 v8, 1.0, v8
	v_add_f32_e32 v5, 1.0, v5
	v_add_f32_e32 v9, 1.0, v9
	v_rcp_f32_e32 v2, v2
	v_rcp_f32_e32 v6, v6
	v_rcp_f32_e32 v3, v3
	v_rcp_f32_e32 v7, v7
	v_rcp_f32_e32 v4, v4
	v_rcp_f32_e32 v8, v8
	v_rcp_f32_e32 v5, v5
	v_rcp_f32_e32 v9, v9
.LBB0_156:
	s_andn2_b64 vcc, exec, s[0:1]
	s_mov_b64 s[0:1], -1
	v_cvt_pk_bf16_f32 v2, v2, v3
	v_cvt_pk_bf16_f32 v3, v4, v5
	v_cvt_pk_bf16_f32 v4, v6, v7
	v_cvt_pk_bf16_f32 v5, v8, v9
	global_store_dwordx4 v[18:19], v[2:5], off offset:256 nt
	s_cbranch_vccnz .LBB0_109
	s_andn2_b64 vcc, exec, s[28:29]
	s_cbranch_vccnz .LBB0_108
	s_barrier
	s_branch .LBB0_108
